# dilated units: deferred epilogue, the tile wait skips the epilogue's own five stores (vmcnt(5))
# baseline (speedup 1.0000x reference)
; #define ATT_WAIT_BAR(N) asm volatile("s_waitcnt vmcnt(" #N ") lgkmcnt(0)\n\ts_barrier" ::: "memory")
; #define ATT_DMA(t, slot) do { glds16(ksrc + (long)(t) * tstep, (unsigned)__builtin_amdgcn_readfirstlane(kdst + (slot))); glds16(vsrc + (long)(t) * tstep, (unsigned)__builtin_amdgcn_readfirstlane(vdst + (slot))); } while (0)
; template <class BIAS>
; __device__ __forceinline__ void attn_tiles(char* shm, const UnitIO& io, int t_begin, int t_end, const BIAS& B, int tid) {
;     ...
;     ATT_DMA(t_begin, 0);
;     asm volatile("" :: "v"(qr[0]), "v"(qr[1]), "v"(qr[2]), "v"(qr[3]));
;     const int nt_ = t_end - t_begin; if (nt_ > 1) ATT_DMA(t_begin + 1, SLOTB); if (nt_ > 2) ATT_DMA(t_begin + 2, 2 * SLOTB);
;     f32x16 o[2]; o[0] = f32x16{}; o[1] = f32x16{}; float l_reg = 0.f;
;     if (nt_ > 2) ATT_WAIT_BAR(4); else if (nt_ > 1) ATT_WAIT_BAR(2); else ATT_WAIT_BAR(0);
.Ldl_ret:
	v_readlane_b32 s62, v191, 0
	v_readlane_b32 s63, v191, 1
	v_readlane_b32 s64, v191, 2
	v_readlane_b32 s65, v191, 3
	v_readlane_b32 s66, v191, 4
	v_readlane_b32 s67, v191, 5
	v_readlane_b32 s75, v191, 6
	s_waitcnt vmcnt(5) lgkmcnt(0)
	s_branch .Ldl_post2
.Ldl_post:
	s_waitcnt vmcnt(0) lgkmcnt(0)
.Ldl_post2:
	v_mov_b32_e32 v190, v191
	v_mov_b32_e32 v2, 0
	s_barrier
	v_mov_b32_e32 v16, v2
	v_mov_b32_e32 v17, v2
	v_mul_f32_e32 v156, 0x42000000, v155
	v_mov_b32_e32 v3, v2
	v_mov_b32_e32 v4, v2
	v_mov_b32_e32 v5, v2
	v_mov_b32_e32 v6, v2
	v_mov_b32_e32 v7, v2
	v_mov_b32_e32 v8, v2
	v_mov_b32_e32 v9, v2
	v_mov_b32_e32 v10, v2
	v_mov_b32_e32 v11, v2
	v_mov_b32_e32 v12, v2
	v_mov_b32_e32 v13, v2
	v_mov_b32_e32 v14, v2
	v_mov_b32_e32 v15, v2
	v_mov_b64_e32 v[32:33], v[16:17]
	v_mul_f32_e32 v149, 0x42800000, v155
	v_mul_f32_e32 v154, 0, v155
	v_writelane_b32 v254, s3, 10
	v_mul_f32_e32 v0, v155, v196
	v_mov_b32_e32 v176, v156
	v_mov_b32_e32 v177, v156
	v_mov_b64_e32 v[30:31], v[14:15]
	v_mov_b64_e32 v[28:29], v[12:13]
	v_mov_b64_e32 v[26:27], v[10:11]
	v_mov_b64_e32 v[24:25], v[8:9]
	v_mov_b64_e32 v[22:23], v[6:7]
	v_mov_b64_e32 v[20:21], v[4:5]
	v_mov_b64_e32 v[18:19], v[2:3]
	v_mov_b32_e32 v151, v2
	s_branch .LBB0_365
